# kvloc tail removed: blocks 0..3 run their meta kvloc unit between the arrive and the wait of grid barrier 1 (projection tasks publish through a ready counter)
# speedup vs baseline: 1.0047x; 1.0047x over previous
.LBB0_288:
	s_waitcnt vmcnt(6)
	v_add_u32_e32 v10, s6, v222
	v_ashrrev_i32_e32 v11, 31, v10
	v_lshlrev_b64 v[10:11], 11, v[10:11]
	v_lshl_add_u64 v[54:55], v[4:5], 0, v[10:11]
	v_add_co_u32_e32 v56, vcc, 0x8000, v54
	global_load_dwordx4 v[10:13], v[54:55], off
	global_load_dwordx4 v[14:17], v[2:3], off
	v_addc_co_u32_e32 v57, vcc, 0, v55, vcc
	v_add_co_u32_e32 v58, vcc, 0x10000, v54
	global_load_dwordx4 v[18:21], v[56:57], off
	s_nop 0
	v_addc_co_u32_e32 v59, vcc, 0, v55, vcc
	v_add_co_u32_e32 v60, vcc, 0x18000, v54
	global_load_dwordx4 v[22:25], v[58:59], off
	s_nop 0
	v_addc_co_u32_e32 v61, vcc, 0, v55, vcc
	global_load_dwordx4 v[26:29], v[60:61], off
	global_load_dwordx4 v[30:33], v[54:55], off offset:64
	global_load_dwordx4 v[34:37], v[2:3], off offset:64
	global_load_dwordx4 v[38:41], v[56:57], off offset:64
	global_load_dwordx4 v[42:45], v[58:59], off offset:64
	global_load_dwordx4 v[46:49], v[60:61], off offset:64
	s_and_b64 vcc, exec, s[4:5]
	s_waitcnt vmcnt(8)
	v_mfma_f32_16x16x32_bf16 v[10:13], v[10:13], v[14:17], 0
	s_waitcnt vmcnt(7)
	v_mfma_f32_16x16x32_bf16 v[18:21], v[18:21], v[14:17], 0
	s_waitcnt vmcnt(6)
	v_mfma_f32_16x16x32_bf16 v[22:25], v[22:25], v[14:17], 0
	s_waitcnt vmcnt(5)
	v_mfma_f32_16x16x32_bf16 v[14:17], v[26:29], v[14:17], 0
	global_load_dwordx4 v[26:29], v[54:55], off offset:128
	global_load_dwordx4 v[50:53], v[2:3], off offset:128
	s_waitcnt vmcnt(5)
	v_mfma_f32_16x16x32_bf16 v[10:13], v[30:33], v[34:37], v[10:13]
	global_load_dwordx4 v[30:33], v[56:57], off offset:128
	s_waitcnt vmcnt(5)
	v_mfma_f32_16x16x32_bf16 v[18:21], v[38:41], v[34:37], v[18:21]
	global_load_dwordx4 v[38:41], v[58:59], off offset:128
	s_waitcnt vmcnt(5)
	v_mfma_f32_16x16x32_bf16 v[22:25], v[42:45], v[34:37], v[22:25]
	global_load_dwordx4 v[42:45], v[60:61], off offset:128
	s_waitcnt vmcnt(5)
	v_mfma_f32_16x16x32_bf16 v[14:17], v[46:49], v[34:37], v[14:17]
	global_load_dwordx4 v[34:37], v[54:55], off offset:192
	global_load_dwordx4 v[46:49], v[2:3], off offset:192
	s_waitcnt vmcnt(5)
	v_mfma_f32_16x16x32_bf16 v[10:13], v[26:29], v[50:53], v[10:13]
	global_load_dwordx4 v[26:29], v[56:57], off offset:192
	s_waitcnt vmcnt(5)
	v_mfma_f32_16x16x32_bf16 v[18:21], v[30:33], v[50:53], v[18:21]
	global_load_dwordx4 v[30:33], v[58:59], off offset:192
	s_waitcnt vmcnt(5)
	v_mfma_f32_16x16x32_bf16 v[22:25], v[38:41], v[50:53], v[22:25]
	global_load_dwordx4 v[38:41], v[60:61], off offset:192
	s_barrier
	s_waitcnt vmcnt(5)
	v_mfma_f32_16x16x32_bf16 v[14:17], v[42:45], v[50:53], v[14:17]
	s_waitcnt vmcnt(3)
	v_mfma_f32_16x16x32_bf16 v[10:13], v[34:37], v[46:49], v[10:13]
	s_waitcnt vmcnt(2)
	v_mfma_f32_16x16x32_bf16 v[18:21], v[26:29], v[46:49], v[18:21]
	s_waitcnt vmcnt(1)
	v_mfma_f32_16x16x32_bf16 v[22:25], v[30:33], v[46:49], v[22:25]
	s_waitcnt vmcnt(0)
	v_mfma_f32_16x16x32_bf16 v[14:17], v[38:41], v[46:49], v[14:17]
	s_nop 1
	ds_write_b128 v8, v[10:13]
	s_nop 0
	ds_write_b128 v8, v[18:21] offset:1024
	s_nop 0
	ds_write_b128 v8, v[22:25] offset:2048
	s_nop 0
	ds_write_b128 v8, v[14:17] offset:3072
	s_waitcnt lgkmcnt(0)
	s_barrier
	s_cbranch_vccnz .LBB0_287
	ds_read_b128 v[10:13], v1
	ds_read_b128 v[14:17], v1 offset:4096
	ds_read_b128 v[18:21], v1 offset:8192
	ds_read_b128 v[22:25], v1 offset:1024
	ds_read_b128 v[26:29], v1 offset:5120
	s_cmp_lt_i32 s11, 8
	s_waitcnt lgkmcnt(3)
	v_pk_add_f32 v[30:31], v[12:13], v[16:17]
	v_pk_add_f32 v[32:33], v[10:11], v[14:15]
	ds_read_b128 v[10:13], v1 offset:12288
	ds_read_b128 v[14:17], v1 offset:9216
	s_waitcnt lgkmcnt(4)
	v_pk_add_f32 v[34:35], v[30:31], v[20:21]
	v_pk_add_f32 v[36:37], v[32:33], v[18:19]
	ds_read_b128 v[18:21], v1 offset:16384
	ds_read_b128 v[30:33], v1 offset:13312
	s_waitcnt lgkmcnt(3)
	v_pk_add_f32 v[38:39], v[34:35], v[12:13]
	v_pk_add_f32 v[40:41], v[36:37], v[10:11]
	ds_read_b128 v[10:13], v1 offset:20480
	ds_read_b128 v[34:37], v1 offset:17408
	s_waitcnt lgkmcnt(3)
	v_pk_add_f32 v[42:43], v[38:39], v[20:21]
	v_pk_add_f32 v[44:45], v[40:41], v[18:19]
	ds_read_b128 v[18:21], v1 offset:24576
	ds_read_b128 v[38:41], v1 offset:21504
	s_waitcnt lgkmcnt(3)
	v_pk_add_f32 v[46:47], v[42:43], v[12:13]
	v_pk_add_f32 v[48:49], v[44:45], v[10:11]
	ds_read_b128 v[10:13], v1 offset:28672
	ds_read_b128 v[42:45], v1 offset:25600
	s_waitcnt lgkmcnt(3)
	v_pk_add_f32 v[48:49], v[48:49], v[18:19]
	v_pk_add_f32 v[46:47], v[46:47], v[20:21]
	ds_read_b128 v[18:21], v1 offset:29696
	s_waitcnt lgkmcnt(2)
	v_pk_add_f32 v[48:49], v[48:49], v[10:11]
	v_pk_add_f32 v[10:11], v[24:25], v[28:29]
	v_pk_add_f32 v[46:47], v[46:47], v[12:13]
	v_pk_add_f32 v[12:13], v[22:23], v[26:27]
	v_pk_add_f32 v[10:11], v[10:11], v[16:17]
	v_pk_add_f32 v[12:13], v[12:13], v[14:15]
	v_pk_add_f32 v[10:11], v[10:11], v[32:33]
	v_pk_add_f32 v[12:13], v[12:13], v[30:31]
	v_pk_add_f32 v[10:11], v[10:11], v[36:37]
	v_pk_add_f32 v[12:13], v[12:13], v[34:35]
	v_pk_add_f32 v[10:11], v[10:11], v[40:41]
	v_pk_add_f32 v[12:13], v[12:13], v[38:39]
	s_waitcnt lgkmcnt(1)
	v_pk_add_f32 v[10:11], v[10:11], v[44:45]
	v_pk_add_f32 v[22:23], v[12:13], v[42:43]
	s_waitcnt lgkmcnt(0)
	v_pk_add_f32 v[50:51], v[10:11], v[20:21]
	ds_read_b128 v[10:13], v1 offset:2048
	ds_read_b128 v[14:17], v1 offset:6144
	v_pk_add_f32 v[52:53], v[22:23], v[18:19]
	ds_read_b128 v[18:21], v1 offset:10240
	ds_read_b128 v[22:25], v1 offset:3072
	ds_read_b128 v[26:29], v1 offset:7168
	s_cselect_b64 vcc, -1, 0
	s_ashr_i32 s7, s6, 31
	s_waitcnt lgkmcnt(3)
	v_pk_add_f32 v[30:31], v[12:13], v[16:17]
	v_pk_add_f32 v[32:33], v[10:11], v[14:15]
	ds_read_b128 v[10:13], v1 offset:14336
	ds_read_b128 v[14:17], v1 offset:11264
	s_waitcnt lgkmcnt(4)
	v_pk_add_f32 v[34:35], v[30:31], v[20:21]
	v_pk_add_f32 v[36:37], v[32:33], v[18:19]
	ds_read_b128 v[18:21], v1 offset:18432
	ds_read_b128 v[30:33], v1 offset:15360
	s_waitcnt lgkmcnt(3)
	v_pk_add_f32 v[38:39], v[34:35], v[12:13]
	v_pk_add_f32 v[40:41], v[36:37], v[10:11]
	ds_read_b128 v[10:13], v1 offset:22528
	ds_read_b128 v[34:37], v1 offset:19456
	s_waitcnt lgkmcnt(3)
	v_pk_add_f32 v[42:43], v[38:39], v[20:21]
	v_pk_add_f32 v[44:45], v[40:41], v[18:19]
	ds_read_b128 v[18:21], v1 offset:26624
	ds_read_b128 v[38:41], v1 offset:23552
	s_waitcnt lgkmcnt(3)
	v_pk_add_f32 v[54:55], v[42:43], v[12:13]
	v_pk_add_f32 v[56:57], v[44:45], v[10:11]
	ds_read_b128 v[10:13], v1 offset:30720
	ds_read_b128 v[42:45], v1 offset:27648
	v_pk_add_f32 v[22:23], v[22:23], v[26:27]
	s_waitcnt lgkmcnt(3)
	v_pk_add_f32 v[54:55], v[54:55], v[20:21]
	v_pk_add_f32 v[56:57], v[56:57], v[18:19]
	ds_read_b128 v[18:21], v1 offset:31744
	v_pk_add_f32 v[14:15], v[22:23], v[14:15]
	v_pk_add_f32 v[24:25], v[24:25], v[28:29]
	v_pk_add_f32 v[14:15], v[14:15], v[30:31]
	v_pk_add_f32 v[16:17], v[24:25], v[16:17]
	v_pk_add_f32 v[14:15], v[14:15], v[34:35]
	v_pk_add_f32 v[16:17], v[16:17], v[32:33]
	s_waitcnt lgkmcnt(3)
	v_pk_add_f32 v[14:15], v[14:15], v[38:39]
	v_pk_add_f32 v[16:17], v[16:17], v[36:37]
	s_waitcnt lgkmcnt(1)
	v_pk_add_f32 v[14:15], v[14:15], v[42:43]
	v_pk_add_f32 v[16:17], v[16:17], v[40:41]
	s_waitcnt lgkmcnt(0)
	v_pk_add_f32 v[14:15], v[14:15], v[18:19]
	v_cndmask_b32_e32 v18, 1.0, v9, vcc
	v_pk_mul_f32 v[24:25], v[18:19], v[48:49] op_sel_hi:[0,1]
	v_pk_mul_f32 v[22:23], v[18:19], v[46:47] op_sel_hi:[0,1]
	v_bfe_u32 v19, v24, 16, 1
	v_add3_u32 v19, v24, v19, s9
	v_bfe_u32 v24, v25, 16, 1
	v_lshrrev_b32_e32 v19, 16, v19
	v_add3_u32 v24, v25, v24, s9
	v_and_or_b32 v24, v24, s10, v19
	v_bfe_u32 v19, v22, 16, 1
	v_add3_u32 v19, v22, v19, s9
	v_bfe_u32 v22, v23, 16, 1
	v_pk_add_f32 v[16:17], v[16:17], v[44:45]
	v_lshrrev_b32_e32 v19, 16, v19
	v_add3_u32 v22, v23, v22, s9
	v_pk_add_f32 v[16:17], v[16:17], v[20:21]
	v_lshl_add_u64 v[20:21], s[6:7], 1, v[6:7]
	v_and_or_b32 v25, v22, s10, v19
	global_store_dwordx2 v[20:21], v[24:25], off sc1
	v_pk_mul_f32 v[24:25], v[18:19], v[52:53] op_sel_hi:[0,1]
	v_pk_mul_f32 v[22:23], v[18:19], v[50:51] op_sel_hi:[0,1]
	v_bfe_u32 v19, v24, 16, 1
	v_add3_u32 v19, v24, v19, s9
	v_bfe_u32 v24, v25, 16, 1
	v_lshrrev_b32_e32 v19, 16, v19
	v_add3_u32 v24, v25, v24, s9
	v_and_or_b32 v24, v24, s10, v19
	v_bfe_u32 v19, v22, 16, 1
	v_add3_u32 v19, v22, v19, s9
	v_pk_add_f32 v[10:11], v[56:57], v[10:11]
	v_lshrrev_b32_e32 v19, 16, v19
	v_bfe_u32 v22, v23, 16, 1
	v_pk_add_f32 v[12:13], v[54:55], v[12:13]
	v_add3_u32 v22, v23, v22, s9
	v_pk_mul_f32 v[10:11], v[18:19], v[10:11] op_sel_hi:[0,1]
	v_and_or_b32 v25, v22, s10, v19
	v_pk_mul_f32 v[12:13], v[18:19], v[12:13] op_sel_hi:[0,1]
	v_bfe_u32 v19, v10, 16, 1
	v_add3_u32 v10, v10, v19, s9
	v_bfe_u32 v19, v11, 16, 1
	v_lshrrev_b32_e32 v10, 16, v10
	v_add3_u32 v11, v11, v19, s9
	v_and_or_b32 v10, v11, s10, v10
	v_bfe_u32 v11, v12, 16, 1
	v_add3_u32 v11, v12, v11, s9
	v_bfe_u32 v12, v13, 16, 1
	v_lshrrev_b32_e32 v11, 16, v11
	v_add3_u32 v12, v13, v12, s9
	v_and_or_b32 v11, v12, s10, v11
	v_pk_mul_f32 v[12:13], v[18:19], v[14:15] op_sel_hi:[0,1]
	v_bfe_u32 v14, v12, 16, 1
	v_add3_u32 v12, v12, v14, s9
	v_bfe_u32 v14, v13, 16, 1
	global_store_dwordx2 v[20:21], v[10:11], off offset:64 sc1
	v_pk_mul_f32 v[10:11], v[18:19], v[16:17] op_sel_hi:[0,1]
	v_lshrrev_b32_e32 v12, 16, v12
	v_add3_u32 v13, v13, v14, s9
	v_and_or_b32 v12, v13, s10, v12
	v_bfe_u32 v13, v10, 16, 1
	v_add3_u32 v10, v10, v13, s9
	v_bfe_u32 v13, v11, 16, 1
	v_lshrrev_b32_e32 v10, 16, v10
	v_add3_u32 v11, v11, v13, s9
	v_and_or_b32 v13, v11, s10, v10
	global_store_dwordx2 v[20:21], v[24:25], off offset:32 sc1
	global_store_dwordx2 v[20:21], v[12:13], off offset:96 sc1
	s_waitcnt vmcnt(0)
	s_mov_b64 exec, 1
	v_mov_b32_e32 v10, 0
	v_mov_b32_e32 v11, 1
	global_atomic_add v10, v11, s[100:101] offset:192
	s_mov_b64 exec, -1
	s_branch .LBB0_287

.Lgb_chk_1:
	v_mov_b32_e32 v11, s89
	v_cmp_lt_u32_e32 vcc, 3, v11
	s_cbranch_vccnz .Lgb_poll_1
	v_mov_b32_e32 v6, 0xc0
	v_mov_b32_e32 v9, 48

.LBB0_360:
	s_cmp_lt_i32 s80, 3
	s_cselect_b64 s[6:7], -1, 0
	s_add_u32 s0, s54, 0x1400000
	s_addc_u32 s1, s55, 0
	s_add_u32 s34, s54, 0xae80000
	s_addc_u32 s35, s55, 0
	s_and_b64 s[36:37], s[6:7], s[4:5]
	s_andn2_b64 vcc, exec, s[36:37]
	v_lshlrev_b32_e32 v158, 3, v0
	v_mbcnt_lo_u32_b32 v227, -1, 0
	v_cmp_gt_u32_e64 s[4:5], 16, v208
	v_cmp_eq_u32_e64 s[6:7], 63, v208
	v_cmp_gt_u32_e64 s[8:9], 32, v208
	v_lshlrev_b32_e32 v250, 4, v0
	v_lshrrev_b32_e32 v225, 1, v0
	v_and_b32_e32 v192, 1, v0
	v_lshrrev_b32_e32 v228, 2, v208
	v_lshlrev_b32_e32 v106, 3, v208
	v_lshlrev_b32_e32 v193, 1, v0
	v_lshrrev_b32_e32 v226, 4, v0
	v_lshrrev_b32_e32 v224, 5, v0
	s_cbranch_vccnz .LBB0_427
	v_mbcnt_hi_u32_b32 v2, -1, v227
	v_and_b32_e32 v3, 64, v2
	v_add_u32_e32 v1, -1, v2
	s_cmp_lt_i32 s89, 4
	v_cmp_lt_i32_e32 vcc, v1, v3
	v_add_u32_e32 v4, -2, v2
	s_cselect_b64 s[38:39], -1, 0
	v_cndmask_b32_e32 v1, v1, v2, vcc
	v_cmp_lt_i32_e32 vcc, v4, v3
	s_cmp_gt_u32 s87, 63
	s_cselect_b64 s[42:43], -1, 0
	v_cndmask_b32_e32 v4, v4, v2, vcc
	s_cmpk_gt_u32 s87, 0x7f
	v_lshlrev_b32_e32 v107, 2, v4
	v_add_u32_e32 v4, -4, v2
	s_cselect_b64 s[44:45], -1, 0
	s_cmpk_gt_u32 s87, 0xbf
	v_cmp_lt_i32_e32 vcc, v4, v3
	s_cselect_b64 s[46:47], -1, 0
	s_cmpk_gt_u32 s87, 0xff
	v_cndmask_b32_e32 v4, v4, v2, vcc
	s_cselect_b64 s[48:49], -1, 0
	s_cmpk_gt_u32 s87, 0x13f
	v_lshlrev_b32_e32 v109, 2, v4
	v_add_u32_e32 v4, -8, v2
	s_cselect_b64 s[50:51], -1, 0
	s_cmpk_gt_u32 s87, 0x17f
	v_cmp_lt_i32_e32 vcc, v4, v3
	s_cselect_b64 s[52:53], -1, 0
	s_cmpk_gt_u32 s87, 0x1bf
	v_cndmask_b32_e32 v4, v4, v2, vcc
	s_cselect_b64 s[54:55], -1, 0
	s_cmpk_gt_u32 s87, 0x1ff
	v_lshlrev_b32_e32 v111, 2, v4
	v_add_u32_e32 v4, -16, v2
	s_cselect_b64 s[56:57], -1, 0
	s_lshl_b32 s22, s89, 3
	v_cmp_lt_i32_e32 vcc, v4, v3
	s_and_b32 s22, s22, 56
	s_ashr_i32 s23, s89, 5
	v_cndmask_b32_e32 v4, v4, v2, vcc
	s_add_i32 s22, s22, s23
	v_lshlrev_b32_e32 v120, 2, v4
	v_subrev_u32_e32 v4, 32, v2
	s_lshr_b32 s24, s22, 3
	v_cmp_lt_i32_e32 vcc, v4, v3
	s_bfe_u32 s23, s89, 0x20003
	s_and_b32 s24, s24, 0x7fffffc
	v_cndmask_b32_e32 v2, v4, v2, vcc
	s_or_b32 s23, s24, s23
	v_lshlrev_b32_e32 v121, 2, v2
	s_lshl_b32 s23, s23, 5
	s_and_b32 s22, s22, 31
	v_lshlrev_b32_e32 v2, 4, v0
	s_or_b32 s67, s23, s22
	s_lshl_b32 s22, s92, 2
	v_and_b32_e32 v3, 0xf0, v2
	v_and_b32_e32 v2, 0x1f0, v2
	s_movk_i32 s24, 0x230
	s_add_i32 s68, s22, 0
	v_add_u32_e32 v5, 0, v2
	v_mov_b32_e32 v2, 0x3f80
	v_cmp_eq_u32_e32 vcc, 0, v192
	s_waitcnt vmcnt(0)
	v_mad_u32_u24 v7, v225, s24, 0
	s_mul_i32 s24, s92, 28
	v_cndmask_b32_e32 v18, 0, v2, vcc
	s_add_i32 s24, s68, s24
	v_and_b32_e32 v2, 24, v225
	v_and_or_b32 v2, v228, 3, v2
	s_movk_i32 s25, 0x110
	v_mov_b32_e32 v4, s24
	v_mad_u32_u24 v11, v2, s25, v4
	s_mul_i32 s25, s92, 0x21e0
	s_add_i32 s26, s24, s25
	v_and_b32_e32 v4, 30, v193
	v_and_b32_e32 v13, 24, v106
	v_mul_u32_u24_e32 v2, 0x230, v2
	v_add_u32_e32 v15, s26, v4
	v_or_b32_e32 v4, 0x200, v0
	s_add_i32 s66, s89, 0x100
	v_add3_u32 v123, 0, v2, v13
	v_and_b32_e32 v2, 12, v228
	s_lshl_b32 s24, s92, 4
	s_mul_i32 s25, s92, 0x2200
	s_movk_i32 s27, 0x220
	v_lshrrev_b32_e32 v124, 4, v4
	v_lshrrev_b32_e32 v125, 5, v4
	v_or_b32_e32 v4, 0x600, v0
	v_and_b32_e32 v108, 0x78, v158
	v_mov_b32_e32 v6, 0
	s_mul_hi_u32 s24, s24, 0x220
	s_add_u32 s69, s34, s25
	v_lshrrev_b32_e32 v127, 5, v4
	v_mad_u32_u24 v128, v2, s27, v15
	v_or_b32_e32 v2, 3, v228
	v_or_b32_e32 v4, 64, v208
	v_or_b32_e32 v8, 0x80, v208
	v_or_b32_e32 v10, 0xc0, v208
	v_or_b32_e32 v12, 0x100, v208
	v_or_b32_e32 v14, 0x140, v208
	v_or_b32_e32 v16, 0x180, v208
	v_or_b32_e32 v22, 0x1c0, v208
	v_or_b32_e32 v24, 0x200, v208
	v_and_b32_e32 v110, 0xf8, v158
	s_addc_u32 s70, s35, s24
	v_mul_u32_u24_e32 v29, 0x220, v2
	v_lshlrev_b32_e32 v2, 3, v4
	v_lshlrev_b32_e32 v31, 4, v4
	v_lshlrev_b32_e32 v4, 3, v8
	v_lshlrev_b32_e32 v32, 4, v8
	v_lshlrev_b32_e32 v8, 3, v10
	v_lshlrev_b32_e32 v33, 4, v10
	v_lshlrev_b32_e32 v10, 3, v12
	v_lshlrev_b32_e32 v34, 4, v12
	v_lshlrev_b32_e32 v12, 3, v14
	v_lshlrev_b32_e32 v35, 4, v14
	v_lshlrev_b32_e32 v14, 3, v16
	v_lshlrev_b32_e32 v36, 4, v16
	v_lshlrev_b32_e32 v16, 3, v22
	v_lshlrev_b32_e32 v37, 4, v22
	v_cmp_gt_u32_e64 s[24:25], s27, v24
	v_lshlrev_b32_e32 v22, 3, v24
	v_lshlrev_b32_e32 v38, 4, v24
	v_lshlrev_b32_e32 v24, 1, v108
	v_mov_b32_e32 v25, v6
	s_movk_i32 s10, 0x100
	s_movk_i32 s20, 0xff
	v_add_u32_e32 v3, 0, v3
	s_movk_i32 s22, 0x80
	v_lshlrev_b32_e32 v9, 4, v192
	v_mul_u32_u24_e32 v17, 0x110, v226
	v_mul_u32_u24_e32 v23, 0x110, v124
	v_mul_u32_u24_e32 v26, 0x230, v224
	v_mul_u32_u24_e32 v27, 0x230, v125
	v_mul_u32_u24_e32 v28, 0x230, v127
	v_lshlrev_b32_e32 v30, 4, v208
	v_lshl_add_u64 v[112:113], s[82:83], 0, v[24:25]
	v_lshlrev_b32_e32 v24, 1, v110
	v_cmp_gt_u32_e64 s[10:11], s10, v0
	s_mov_b32 s41, 0
	v_lshlrev_b32_e32 v1, 2, v1
	v_cmp_eq_u32_e64 s[12:13], 0, v208
	v_cmp_gt_u32_e64 s[14:15], 2, v208
	v_cmp_gt_u32_e64 s[16:17], 4, v208
	v_cmp_gt_u32_e64 s[18:19], 8, v208
	v_cmp_eq_u32_e64 s[20:21], s20, v0
	v_lshl_add_u32 v122, v0, 2, 0
	v_cmp_gt_u32_e64 s[22:23], s22, v0
	v_mov_b32_e32 v19, v6
	v_mov_b32_e32 v20, v6
	v_mov_b32_e32 v21, v6
	v_or_b32_e32 v126, 32, v224
	v_lshl_add_u64 v[114:115], s[82:83], 0, v[24:25]
	v_or_b32_e32 v129, 64, v127
	v_or_b32_e32 v130, 64, v125
	v_or_b32_e32 v131, 64, v124
	v_or_b32_e32 v132, 64, v226
	v_lshl_add_u32 v133, v124, 2, 0
	v_lshl_add_u32 v134, v226, 2, 0
	s_xor_b64 s[58:59], s[38:39], -1
	s_movk_i32 s71, 0x1800
	s_mov_b32 s72, 0xffff0000
	s_movk_i32 s73, 0x7fff
	v_add_u32_e32 v135, v3, v17
	v_add_u32_e32 v136, v3, v23
	v_add_u32_e32 v137, v5, v26
	v_add_u32_e32 v138, v5, v27
	v_add_u32_e32 v139, v5, v28
	v_add_u32_e32 v140, v7, v9
	v_add_u32_e32 v141, v11, v13
	v_add_u32_e32 v142, v15, v29
	v_lshlrev_b32_e32 v143, 1, v106
	v_add_u32_e32 v144, s26, v30
	v_lshlrev_b32_e32 v145, 1, v2
	v_add_u32_e32 v146, s26, v31
	v_lshlrev_b32_e32 v147, 1, v4
	v_add_u32_e32 v148, s26, v32
	v_lshlrev_b32_e32 v149, 1, v8
	v_add_u32_e32 v150, s26, v33
	v_lshlrev_b32_e32 v151, 1, v10
	v_add_u32_e32 v152, s26, v34
	v_lshlrev_b32_e32 v153, 1, v12
	v_add_u32_e32 v154, s26, v35
	v_lshlrev_b32_e32 v155, 1, v14
	v_add_u32_e32 v156, s26, v36
	v_lshlrev_b32_e32 v157, 1, v16
	v_add_u32_e32 v159, s26, v37
	v_lshlrev_b32_e32 v160, 1, v22
	v_add_u32_e32 v161, s26, v38
	s_branch .LBB0_363
.LBB0_362:
	s_or_b64 exec, exec, s[60:61]
	s_andn2_b64 s[26:27], s[38:39], s[58:59]
	s_mov_b64 s[58:59], -1
	s_and_b64 vcc, exec, s[26:27]
	s_barrier
	s_cbranch_vccz .LBB0_426
	s_cmp_lg_u32 s92, 0
	s_cbranch_scc1 .Lgw_end_1
	s_mov_b64 exec, 1
	v_mov_b32_e32 v10, 0x22160
	ds_read_b32 v11, v10
	v_mov_b32_e32 v12, s99
	v_lshrrev_b32_e32 v12, 16, v12
	v_mov_b32_e32 v13, s98
	v_min_u32_e32 v13, 8, v13
	v_mov_b32_e32 v14, 0
	s_waitcnt lgkmcnt(0)
	v_mul_lo_u32 v13, v13, v11
.Lgw_poll_1:
	global_load_dword v15, v12, s[100:101] sc1
	v_add_u32_e32 v14, 1, v14
	s_waitcnt vmcnt(0)
	v_cmp_ge_u32_e32 vcc, v15, v13
	s_cbranch_vccnz .Lgw_end_1x
	v_cmp_gt_u32_e32 vcc, 0x80000, v14
	s_sleep 1
	s_cbranch_vccnz .Lgw_poll_1

.Lgw_end_1:
	s_barrier
